# speedup vs baseline: 1.0606x; 1.0110x over previous
_Z11prep_kernelPKfS0_S0_S0_S0_S0_S0_S0_S0_S0_PDv8_DF16_S2_:
	v_lshl_add_u32 v4, s2, 8, v0
	s_mov_b32 s2, 0x50fff
	v_cmp_lt_i32_e32 vcc, s2, v4
	s_and_saveexec_b64 s[2:3], vcc
	s_xor_b64 s[2:3], exec, s[2:3]
	s_cbranch_execz .LBB0_48
	s_mov_b32 s4, 0x54e00
	v_cmp_gt_u32_e32 vcc, s4, v4
	s_and_saveexec_b64 s[4:5], vcc
	s_cbranch_execz .LBB0_47
	s_load_dwordx2 s[6:7], s[0:1], 0x50
	v_add_u32_e32 v1, 0xfffaf000, v4
	v_lshrrev_b32_e32 v2, 6, v1
	s_movk_i32 s8, 0x19ff
	v_add_u32_e32 v3, 0xb00, v2
	v_cmp_lt_u32_e32 vcc, s8, v1
	s_movk_i32 s8, 0x67
	v_and_b32_e32 v7, 31, v0
	v_cndmask_b32_e32 v1, v2, v3, vcc
	v_bfe_u32 v6, v0, 5, 1
	v_cmp_lt_u32_e32 vcc, s8, v1
	s_and_saveexec_b64 s[8:9], vcc
	s_xor_b64 s[8:9], exec, s[8:9]
	s_cbranch_execz .LBB0_44
	s_movk_i32 s10, 0xb77
	v_cmp_lt_u32_e32 vcc, s10, v1
	s_and_saveexec_b64 s[10:11], vcc
	s_xor_b64 s[10:11], exec, s[10:11]
	s_cbranch_execz .LBB0_25
	s_movk_i32 s12, 0xbb7
	v_cmp_lt_u32_e32 vcc, s12, v1
	s_and_saveexec_b64 s[12:13], vcc
	s_xor_b64 s[12:13], exec, s[12:13]
	s_cbranch_execz .LBB0_22
	s_load_dwordx2 s[14:15], s[0:1], 0x28
	v_add_u32_e32 v3, 0xfffff448, v1
	v_lshlrev_b32_e32 v2, 3, v3
	v_lshlrev_b32_e32 v3, 2, v3
	s_movk_i32 s16, 0x60
	v_and_b32_e32 v4, 0x7fffffc0, v3
	v_lshlrev_b32_e32 v3, 4, v1
	v_and_or_b32 v2, v2, s16, v7
	s_movk_i32 s18, 0x64
	v_and_b32_e32 v5, 48, v3
	v_lshlrev_b32_e32 v6, 2, v6
	v_cmp_gt_u32_e32 vcc, s18, v2
	v_mov_b32_e32 v3, 0
	v_or3_b32 v5, v5, v6, v4
	v_mov_b32_e32 v4, 0
	v_mov_b32_e32 v6, 0
	v_mov_b32_e32 v7, 0
	v_mov_b32_e32 v8, 0
	v_mov_b32_e32 v9, 0
	v_mov_b32_e32 v10, 0
	v_mov_b32_e32 v11, 0
	s_and_saveexec_b64 s[16:17], vcc
	s_cbranch_execz .LBB0_21
	v_mad_u64_u32 v[12:13], s[18:19], v5, s18, v[2:3]
	v_mov_b32_e32 v13, 0
	s_waitcnt lgkmcnt(0)
	v_lshl_add_u64 v[12:13], v[12:13], 2, s[14:15]
	v_add_co_u32_e32 v14, vcc, 0x1130, v12
	s_nop 1
	v_addc_co_u32_e32 v15, vcc, 0, v13, vcc
	global_load_dword v4, v[12:13], off
	global_load_dword v3, v[12:13], off offset:400
	global_load_dword v7, v[12:13], off offset:800
	global_load_dword v6, v[12:13], off offset:1200
	global_load_dword v9, v[12:13], off offset:3200
	global_load_dword v8, v[12:13], off offset:3600
	global_load_dword v10, v[12:13], off offset:4000
	global_load_dword v11, v[14:15], off
	s_waitcnt vmcnt(0)
	v_cvt_f16_f32_e32 v4, v4
	v_cvt_f16_f32_e32 v3, v3
	v_cvt_f16_f32_e32 v7, v7
	v_cvt_f16_f32_e32 v6, v6
	v_cvt_f16_f32_e32 v9, v9
	v_cvt_f16_f32_e32 v8, v8
	v_cvt_f16_f32_e32 v10, v10
	v_cvt_f16_f32_e32 v11, v11

.LBB0_25:
	s_andn2_saveexec_b64 s[10:11], s[10:11]
	s_cbranch_execz .LBB0_43
	v_add_u32_e32 v3, 0xfffff498, v1
	s_load_dwordx2 s[12:13], s[0:1], 0x18
	v_lshrrev_b32_e32 v4, 3, v7
	v_lshrrev_b32_e32 v3, 1, v3
	s_mov_b32 s14, 0x1fffffc
	v_and_or_b32 v3, v3, s14, v4
	v_lshlrev_b32_e32 v4, 7, v3
	v_lshlrev_b32_e32 v3, 4, v1
	v_and_b32_e32 v2, 7, v0
	v_and_b32_e32 v5, 0x70, v3
	v_lshlrev_b32_e32 v6, 2, v6
	v_cmp_gt_u32_e32 vcc, 5, v2
	v_mov_b32_e32 v3, 0
	v_or3_b32 v5, v5, v6, v4
	v_mov_b32_e32 v4, 0
	v_mov_b32_e32 v6, 0
	v_mov_b32_e32 v7, 0
	v_mov_b32_e32 v8, 0
	v_mov_b32_e32 v9, 0
	v_mov_b32_e32 v10, 0
	v_mov_b32_e32 v11, 0
	s_and_saveexec_b64 s[14:15], vcc
	s_cbranch_execz .LBB0_42
	v_mad_u64_u32 v[12:13], s[16:17], v5, 5, v[2:3]
	v_ashrrev_i32_e32 v13, 31, v12
	s_waitcnt lgkmcnt(0)
	v_lshl_add_u64 v[12:13], v[12:13], 2, s[12:13]
	global_load_dword v4, v[12:13], off
	global_load_dword v3, v[12:13], off offset:20
	global_load_dword v7, v[12:13], off offset:40
	global_load_dword v6, v[12:13], off offset:60
	global_load_dword v9, v[12:13], off offset:160
	global_load_dword v8, v[12:13], off offset:180
	global_load_dword v11, v[12:13], off offset:200
	global_load_dword v10, v[12:13], off offset:220
	s_waitcnt vmcnt(0)
	v_cvt_f16_f32_e32 v4, v4
	v_cvt_f16_f32_e32 v3, v3
	v_cvt_f16_f32_e32 v7, v7
	v_cvt_f16_f32_e32 v6, v6
	v_cvt_f16_f32_e32 v9, v9
	v_cvt_f16_f32_e32 v8, v8
	v_cvt_f16_f32_e32 v11, v11
	v_cvt_f16_f32_e32 v10, v10
